# all four GEMM unit loops: first K-loop trip peeled, the first MFMA into each accumulator takes SrcC=0, per-unit accumulator zeroing (64 v_mov_b64) removed (on top of v51)
# speedup vs baseline: 1.0040x; 1.0040x over previous
.Lpeel_in:
	s_mov_b64 s[26:27], 0
	v_mov_b64_e32 v[178:179], v[174:175]
	v_mov_b64_e32 v[180:181], v[168:169]
	v_mov_b32_e32 v186, v176
	v_mov_b32_e32 v172, v170
	ds_read_b128 v[0:3], v193
	ds_read_b128 v[8:11], v193 offset:2048
	ds_read_b128 v[4:7], v195
	ds_read_b128 v[12:15], v195 offset:2048
	s_add_u32 s15, s24, 0x80
	s_addc_u32 s23, s25, 0
	s_and_b64 s[26:27], s[26:27], exec
	s_cselect_b32 s29, s19, s23
	s_cselect_b32 s28, s18, s15
	s_cselect_b32 s27, s17, s3
	s_cselect_b32 s26, s16, s2
	v_lshl_add_u64 v[16:17], s[24:25], 0, v[168:169]
	s_add_i32 m0, s47, 0xc000
	ds_read_b128 v[218:221], v192
	ds_read_b128 v[226:229], v192 offset:2048
	ds_read_b128 v[222:225], v194
	ds_read_b128 v[230:233], v194 offset:2048
	ds_read_b128 v[234:237], v192 offset:4096
	ds_read_b128 v[242:245], v192 offset:6144
	ds_read_b128 v[238:241], v194 offset:4096
	ds_read_b128 v[246:249], v194 offset:6144
	global_load_lds_dwordx4 v[16:17], off
	v_lshl_add_u64 v[16:17], s[24:25], 0, v[174:175]
	s_add_i32 m0, s47, 0xe000
	s_nop 0
	global_load_lds_dwordx4 v[16:17], off
	s_waitcnt lgkmcnt(8)
	s_barrier
	s_waitcnt lgkmcnt(0)
	s_setprio 1
	s_waitcnt lgkmcnt(0)
	v_mfma_scale_f32_16x16x128_f8f6f4 v[156:159], v[0:7], v[218:225], 0, v191, v191 op_sel_hi:[0,0,0]
	v_mfma_scale_f32_16x16x128_f8f6f4 v[152:155], v[8:15], v[218:225], 0, v191, v191 op_sel_hi:[0,0,0]
	v_mfma_scale_f32_16x16x128_f8f6f4 v[148:151], v[0:7], v[226:233], 0, v191, v191 op_sel_hi:[0,0,0]
	v_mfma_scale_f32_16x16x128_f8f6f4 v[144:147], v[8:15], v[226:233], 0, v191, v191 op_sel_hi:[0,0,0]
	v_mfma_scale_f32_16x16x128_f8f6f4 v[140:143], v[0:7], v[234:241], 0, v191, v191 op_sel_hi:[0,0,0]
	v_mfma_scale_f32_16x16x128_f8f6f4 v[136:139], v[8:15], v[234:241], 0, v191, v191 op_sel_hi:[0,0,0]
	v_mfma_scale_f32_16x16x128_f8f6f4 v[132:135], v[0:7], v[242:249], 0, v191, v191 op_sel_hi:[0,0,0]
	v_mfma_scale_f32_16x16x128_f8f6f4 v[128:131], v[8:15], v[242:249], 0, v191, v191 op_sel_hi:[0,0,0]
	s_setprio 0
	s_barrier
	s_mov_b32 m0, s30
	v_lshl_add_u64 v[182:183], s[26:27], 0, v[162:163]
	ds_read_b128 v[16:19], v193 offset:16384
	ds_read_b128 v[24:27], v193 offset:18432
	ds_read_b128 v[20:23], v195 offset:16384
	ds_read_b128 v[28:31], v195 offset:18432
	global_load_lds_dwordx4 v[182:183], off
	v_lshl_add_u64 v[184:185], s[26:27], 0, v[164:165]
	s_mov_b32 m0, s46
	s_nop 0
	global_load_lds_dwordx4 v[184:185], off
	s_barrier
	s_waitcnt lgkmcnt(0)
	s_setprio 1
	s_waitcnt lgkmcnt(0)
	v_mfma_scale_f32_16x16x128_f8f6f4 v[92:95], v[16:23], v[218:225], 0, v191, v191 op_sel_hi:[0,0,0]
	v_mfma_scale_f32_16x16x128_f8f6f4 v[88:91], v[24:31], v[218:225], 0, v191, v191 op_sel_hi:[0,0,0]
	v_mfma_scale_f32_16x16x128_f8f6f4 v[84:87], v[16:23], v[226:233], 0, v191, v191 op_sel_hi:[0,0,0]
	v_mfma_scale_f32_16x16x128_f8f6f4 v[80:83], v[24:31], v[226:233], 0, v191, v191 op_sel_hi:[0,0,0]
	v_mfma_scale_f32_16x16x128_f8f6f4 v[76:79], v[16:23], v[234:241], 0, v191, v191 op_sel_hi:[0,0,0]
	v_mfma_scale_f32_16x16x128_f8f6f4 v[72:75], v[24:31], v[234:241], 0, v191, v191 op_sel_hi:[0,0,0]
	v_mfma_scale_f32_16x16x128_f8f6f4 v[68:71], v[16:23], v[242:249], 0, v191, v191 op_sel_hi:[0,0,0]
	v_mfma_scale_f32_16x16x128_f8f6f4 v[64:67], v[24:31], v[242:249], 0, v191, v191 op_sel_hi:[0,0,0]
	s_setprio 0
	s_mov_b32 m0, s47
	s_barrier
	ds_read_b128 v[218:221], v192 offset:16384
	ds_read_b128 v[226:229], v192 offset:18432
	ds_read_b128 v[222:225], v194 offset:16384
	ds_read_b128 v[230:233], v194 offset:18432
	ds_read_b128 v[234:237], v192 offset:20480
	ds_read_b128 v[242:245], v192 offset:22528
	ds_read_b128 v[238:241], v194 offset:20480
	ds_read_b128 v[246:249], v194 offset:22528
	global_load_lds_dwordx4 v172, s[28:29]
	s_mov_b32 m0, s83
	v_mov_b32_e32 v187, v173
	global_load_lds_dwordx4 v186, s[28:29]
	s_barrier
	s_waitcnt lgkmcnt(0)
	v_lshl_add_u64 v[188:189], s[28:29], 0, v[172:173]
	v_lshl_add_u64 v[186:187], s[28:29], 0, v[186:187]
	s_setprio 1
	s_waitcnt lgkmcnt(0)
	v_mfma_scale_f32_16x16x128_f8f6f4 v[124:127], v[0:7], v[218:225], 0, v191, v191 op_sel_hi:[0,0,0]
	v_mfma_scale_f32_16x16x128_f8f6f4 v[120:123], v[8:15], v[218:225], 0, v191, v191 op_sel_hi:[0,0,0]
	v_mfma_scale_f32_16x16x128_f8f6f4 v[116:119], v[0:7], v[226:233], 0, v191, v191 op_sel_hi:[0,0,0]
	v_mfma_scale_f32_16x16x128_f8f6f4 v[112:115], v[8:15], v[226:233], 0, v191, v191 op_sel_hi:[0,0,0]
	v_mfma_scale_f32_16x16x128_f8f6f4 v[108:111], v[0:7], v[234:241], 0, v191, v191 op_sel_hi:[0,0,0]
	v_mfma_scale_f32_16x16x128_f8f6f4 v[104:107], v[8:15], v[234:241], 0, v191, v191 op_sel_hi:[0,0,0]
	v_mfma_scale_f32_16x16x128_f8f6f4 v[100:103], v[0:7], v[242:249], 0, v191, v191 op_sel_hi:[0,0,0]
	v_mfma_scale_f32_16x16x128_f8f6f4 v[96:99], v[8:15], v[242:249], 0, v191, v191 op_sel_hi:[0,0,0]
	s_setprio 0
	s_barrier
	s_add_u32 s72, s26, 0x20000
	s_addc_u32 s73, s27, 0
	s_mov_b32 m0, s82
	v_lshl_add_u64 v[0:1], s[72:73], 0, v[162:163]
	global_load_lds_dwordx4 v[0:1], off
	v_lshl_add_u64 v[0:1], s[72:73], 0, v[164:165]
	s_mov_b32 m0, s80
	s_nop 0
	global_load_lds_dwordx4 v[0:1], off
	s_waitcnt vmcnt(6)
	s_barrier
	s_setprio 1
	v_mfma_scale_f32_16x16x128_f8f6f4 v[60:63], v[16:23], v[218:225], 0, v191, v191 op_sel_hi:[0,0,0]
	v_mfma_scale_f32_16x16x128_f8f6f4 v[56:59], v[24:31], v[218:225], 0, v191, v191 op_sel_hi:[0,0,0]
	v_mfma_scale_f32_16x16x128_f8f6f4 v[52:55], v[16:23], v[226:233], 0, v191, v191 op_sel_hi:[0,0,0]
	v_mfma_scale_f32_16x16x128_f8f6f4 v[48:51], v[24:31], v[226:233], 0, v191, v191 op_sel_hi:[0,0,0]
	v_mfma_scale_f32_16x16x128_f8f6f4 v[44:47], v[16:23], v[234:241], 0, v191, v191 op_sel_hi:[0,0,0]
	v_mfma_scale_f32_16x16x128_f8f6f4 v[40:43], v[24:31], v[234:241], 0, v191, v191 op_sel_hi:[0,0,0]
	v_mfma_scale_f32_16x16x128_f8f6f4 v[36:39], v[16:23], v[242:249], 0, v191, v191 op_sel_hi:[0,0,0]
	v_mfma_scale_f32_16x16x128_f8f6f4 v[32:35], v[24:31], v[242:249], 0, v191, v191 op_sel_hi:[0,0,0]
	s_setprio 0
	s_barrier
	ds_read_b128 v[0:3], v193 offset:32768
	ds_read_b128 v[8:11], v193 offset:34816
	ds_read_b128 v[4:7], v195 offset:32768
	ds_read_b128 v[12:15], v195 offset:34816
	s_mov_b32 m0, s81
	v_lshl_add_u64 v[180:181], s[28:29], 0, v[180:181]
	ds_read_b128 v[16:19], v192 offset:32768
	ds_read_b128 v[24:27], v192 offset:34816
	ds_read_b128 v[20:23], v194 offset:32768
	ds_read_b128 v[28:31], v194 offset:34816
	ds_read_b128 v[218:221], v192 offset:36864
	ds_read_b128 v[226:229], v192 offset:38912
	ds_read_b128 v[222:225], v194 offset:36864
	ds_read_b128 v[230:233], v194 offset:38912
	global_load_lds_dwordx4 v[180:181], off
	v_lshl_add_u64 v[178:179], s[28:29], 0, v[178:179]
	s_mov_b32 m0, s50
	s_nop 0
	global_load_lds_dwordx4 v[178:179], off
	s_waitcnt lgkmcnt(8)
	s_barrier
	s_waitcnt lgkmcnt(0)
	s_setprio 1
	s_waitcnt lgkmcnt(0)
	v_mfma_scale_f32_16x16x128_f8f6f4 v[156:159], v[0:7], v[16:23], v[156:159], v191, v191 op_sel_hi:[0,0,0]
	v_mfma_scale_f32_16x16x128_f8f6f4 v[152:155], v[8:15], v[16:23], v[152:155], v191, v191 op_sel_hi:[0,0,0]
	v_mfma_scale_f32_16x16x128_f8f6f4 v[148:151], v[0:7], v[24:31], v[148:151], v191, v191 op_sel_hi:[0,0,0]
	v_mfma_scale_f32_16x16x128_f8f6f4 v[144:147], v[8:15], v[24:31], v[144:147], v191, v191 op_sel_hi:[0,0,0]
	v_mfma_scale_f32_16x16x128_f8f6f4 v[140:143], v[0:7], v[218:225], v[140:143], v191, v191 op_sel_hi:[0,0,0]
	v_mfma_scale_f32_16x16x128_f8f6f4 v[136:139], v[8:15], v[218:225], v[136:139], v191, v191 op_sel_hi:[0,0,0]
	v_mfma_scale_f32_16x16x128_f8f6f4 v[132:135], v[0:7], v[226:233], v[132:135], v191, v191 op_sel_hi:[0,0,0]
	v_mfma_scale_f32_16x16x128_f8f6f4 v[128:131], v[8:15], v[226:233], v[128:131], v191, v191 op_sel_hi:[0,0,0]
	s_setprio 0
	s_barrier
	s_mov_b32 m0, s51
	v_lshl_add_u64 v[178:179], v[182:183], 0, s[40:41]
	ds_read_b128 v[234:237], v193 offset:49152
	ds_read_b128 v[242:245], v193 offset:51200
	ds_read_b128 v[238:241], v195 offset:49152
	ds_read_b128 v[246:249], v195 offset:51200
	global_load_lds_dwordx4 v[178:179], off
	v_lshl_add_u64 v[178:179], v[184:185], 0, s[40:41]
	s_mov_b32 m0, s70
	s_nop 0
	global_load_lds_dwordx4 v[178:179], off
	s_barrier
	s_waitcnt lgkmcnt(0)
	s_setprio 1
	s_waitcnt lgkmcnt(0)
	v_mfma_scale_f32_16x16x128_f8f6f4 v[92:95], v[234:241], v[16:23], v[92:95], v191, v191 op_sel_hi:[0,0,0]
	v_mfma_scale_f32_16x16x128_f8f6f4 v[88:91], v[242:249], v[16:23], v[88:91], v191, v191 op_sel_hi:[0,0,0]
	v_mfma_scale_f32_16x16x128_f8f6f4 v[84:87], v[234:241], v[24:31], v[84:87], v191, v191 op_sel_hi:[0,0,0]
	v_mfma_scale_f32_16x16x128_f8f6f4 v[80:83], v[242:249], v[24:31], v[80:83], v191, v191 op_sel_hi:[0,0,0]
	v_mfma_scale_f32_16x16x128_f8f6f4 v[76:79], v[234:241], v[218:225], v[76:79], v191, v191 op_sel_hi:[0,0,0]
	v_mfma_scale_f32_16x16x128_f8f6f4 v[72:75], v[242:249], v[218:225], v[72:75], v191, v191 op_sel_hi:[0,0,0]
	v_mfma_scale_f32_16x16x128_f8f6f4 v[68:71], v[234:241], v[226:233], v[68:71], v191, v191 op_sel_hi:[0,0,0]
	v_mfma_scale_f32_16x16x128_f8f6f4 v[64:67], v[242:249], v[226:233], v[64:67], v191, v191 op_sel_hi:[0,0,0]
	s_setprio 0
	s_mov_b32 m0, s71
	v_lshl_add_u64 v[188:189], v[188:189], 0, s[40:41]
	s_barrier
	ds_read_b128 v[16:19], v192 offset:49152
	ds_read_b128 v[24:27], v192 offset:51200
	ds_read_b128 v[20:23], v194 offset:49152
	ds_read_b128 v[28:31], v194 offset:51200
	ds_read_b128 v[178:181], v192 offset:53248
	ds_read_b128 v[218:221], v192 offset:55296
	ds_read_b128 v[182:185], v194 offset:53248
	ds_read_b128 v[222:225], v194 offset:55296
	global_load_lds_dwordx4 v[188:189], off
	v_lshl_add_u64 v[186:187], v[186:187], 0, s[40:41]
	s_mov_b32 m0, s87
	s_nop 0
	global_load_lds_dwordx4 v[186:187], off
	s_barrier
	s_waitcnt lgkmcnt(0)
	s_setprio 1
	s_waitcnt lgkmcnt(0)
	v_mfma_scale_f32_16x16x128_f8f6f4 v[124:127], v[0:7], v[16:23], v[124:127], v191, v191 op_sel_hi:[0,0,0]
	v_mfma_scale_f32_16x16x128_f8f6f4 v[120:123], v[8:15], v[16:23], v[120:123], v191, v191 op_sel_hi:[0,0,0]
	v_mfma_scale_f32_16x16x128_f8f6f4 v[116:119], v[0:7], v[24:31], v[116:119], v191, v191 op_sel_hi:[0,0,0]
	v_mfma_scale_f32_16x16x128_f8f6f4 v[112:115], v[8:15], v[24:31], v[112:115], v191, v191 op_sel_hi:[0,0,0]
	v_mfma_scale_f32_16x16x128_f8f6f4 v[108:111], v[0:7], v[178:185], v[108:111], v191, v191 op_sel_hi:[0,0,0]
	v_mfma_scale_f32_16x16x128_f8f6f4 v[104:107], v[8:15], v[178:185], v[104:107], v191, v191 op_sel_hi:[0,0,0]
	v_mfma_scale_f32_16x16x128_f8f6f4 v[100:103], v[0:7], v[218:225], v[100:103], v191, v191 op_sel_hi:[0,0,0]
	v_mfma_scale_f32_16x16x128_f8f6f4 v[96:99], v[8:15], v[218:225], v[96:99], v191, v191 op_sel_hi:[0,0,0]
	s_setprio 0
	s_barrier
	s_add_u32 s26, s26, 0x20080
	s_addc_u32 s27, s27, 0
	s_mov_b32 m0, s1
	v_lshl_add_u64 v[0:1], s[26:27], 0, v[162:163]
	global_load_lds_dwordx4 v[0:1], off
	v_lshl_add_u64 v[0:1], s[26:27], 0, v[164:165]
	s_mov_b32 m0, s56
	s_nop 0
	global_load_lds_dwordx4 v[0:1], off
	s_waitcnt vmcnt(6)
	s_barrier
	s_setprio 1
	v_mfma_scale_f32_16x16x128_f8f6f4 v[60:63], v[234:241], v[16:23], v[60:63], v191, v191 op_sel_hi:[0,0,0]
	v_mfma_scale_f32_16x16x128_f8f6f4 v[56:59], v[242:249], v[16:23], v[56:59], v191, v191 op_sel_hi:[0,0,0]
	v_mfma_scale_f32_16x16x128_f8f6f4 v[52:55], v[234:241], v[24:31], v[52:55], v191, v191 op_sel_hi:[0,0,0]
	v_mfma_scale_f32_16x16x128_f8f6f4 v[48:51], v[242:249], v[24:31], v[48:51], v191, v191 op_sel_hi:[0,0,0]
	v_mfma_scale_f32_16x16x128_f8f6f4 v[44:47], v[234:241], v[178:185], v[44:47], v191, v191 op_sel_hi:[0,0,0]
	v_mfma_scale_f32_16x16x128_f8f6f4 v[40:43], v[242:249], v[178:185], v[40:43], v191, v191 op_sel_hi:[0,0,0]
	v_mfma_scale_f32_16x16x128_f8f6f4 v[36:39], v[234:241], v[218:225], v[36:39], v191, v191 op_sel_hi:[0,0,0]
	v_mfma_scale_f32_16x16x128_f8f6f4 v[32:35], v[242:249], v[218:225], v[32:35], v191, v191 op_sel_hi:[0,0,0]
	s_setprio 0
	s_add_i32 s13, s13, 2
	s_add_u32 s24, s24, 0x100
	s_addc_u32 s25, s25, 0
	s_add_u32 s2, s2, 0x100
	s_addc_u32 s3, s3, 0
	s_cmp_gt_u32 s13, 5
	s_barrier
	s_branch .LBB0_539

.Lpeel_out:
	s_mov_b64 s[28:29], 0
	v_mov_b64_e32 v[136:137], v[132:133]
	v_mov_b64_e32 v[138:139], v[128:129]
	v_mov_b32_e32 v172, v130
	v_mov_b32_e32 v140, v134
	ds_read_b128 v[142:145], v186
	ds_read_b128 v[146:149], v186 offset:1024
	ds_read_b128 v[150:153], v186 offset:2048
	ds_read_b128 v[162:165], v186 offset:3072
	s_add_u32 s30, s26, 0x80
	s_addc_u32 s31, s27, 0
	s_and_b64 s[28:29], s[28:29], exec
	s_cselect_b32 s31, s19, s31
	s_cselect_b32 s30, s18, s30
	s_cselect_b32 s29, s17, s15
	s_cselect_b32 s28, s16, s9
	v_lshl_add_u64 v[154:155], s[26:27], 0, v[128:129]
	s_add_i32 m0, s23, 0xc000
	ds_read_b128 v[166:169], v185
	ds_read_b128 v[174:177], v185 offset:1024
	ds_read_b128 v[178:181], v185 offset:2048
	ds_read_b128 v[204:207], v185 offset:3072
	ds_read_b128 v[208:211], v185 offset:4096
	ds_read_b128 v[214:217], v185 offset:5120
	ds_read_b128 v[218:221], v185 offset:6144
	ds_read_b128 v[222:225], v185 offset:7168
	global_load_lds_dwordx4 v[154:155], off
	v_lshl_add_u64 v[154:155], s[26:27], 0, v[132:133]
	s_add_i32 m0, s23, 0xe000
	s_nop 0
	global_load_lds_dwordx4 v[154:155], off
	s_waitcnt lgkmcnt(8)
	s_barrier
	s_waitcnt lgkmcnt(0)
	s_setprio 1
	s_waitcnt lgkmcnt(0)
	v_mfma_f32_16x16x32_bf16 v[124:127], v[142:145], v[166:169], 0
	v_mfma_f32_16x16x32_bf16 v[120:123], v[150:153], v[166:169], 0
	v_mfma_f32_16x16x32_bf16 v[116:119], v[142:145], v[178:181], 0
	v_mfma_f32_16x16x32_bf16 v[112:115], v[150:153], v[178:181], 0
	v_mfma_f32_16x16x32_bf16 v[108:111], v[142:145], v[208:211], 0
	v_mfma_f32_16x16x32_bf16 v[104:107], v[150:153], v[208:211], 0
	v_mfma_f32_16x16x32_bf16 v[100:103], v[142:145], v[218:221], 0
	v_mfma_f32_16x16x32_bf16 v[96:99], v[150:153], v[218:221], 0
	v_mfma_f32_16x16x32_bf16 v[124:127], v[146:149], v[174:177], v[124:127]
	v_mfma_f32_16x16x32_bf16 v[120:123], v[162:165], v[174:177], v[120:123]
	v_mfma_f32_16x16x32_bf16 v[116:119], v[146:149], v[204:207], v[116:119]
	v_mfma_f32_16x16x32_bf16 v[112:115], v[162:165], v[204:207], v[112:115]
	v_mfma_f32_16x16x32_bf16 v[108:111], v[146:149], v[214:217], v[108:111]
	v_mfma_f32_16x16x32_bf16 v[104:107], v[162:165], v[214:217], v[104:107]
	v_mfma_f32_16x16x32_bf16 v[100:103], v[146:149], v[222:225], v[100:103]
	v_mfma_f32_16x16x32_bf16 v[96:99], v[162:165], v[222:225], v[96:99]
	s_setprio 0
	s_barrier
	s_mov_b32 m0, s25
	v_lshl_add_u64 v[170:171], s[28:29], 0, v[158:159]
	ds_read_b128 v[226:229], v186 offset:16384
	ds_read_b128 v[230:233], v186 offset:17408
	ds_read_b128 v[234:237], v186 offset:18432
	ds_read_b128 v[238:241], v186 offset:19456
	global_load_lds_dwordx4 v[170:171], off
	v_lshl_add_u64 v[182:183], s[28:29], 0, v[160:161]
	s_mov_b32 m0, s51
	s_nop 0
	global_load_lds_dwordx4 v[182:183], off
	s_barrier
	s_waitcnt lgkmcnt(0)
	s_setprio 1
	s_waitcnt lgkmcnt(0)
	v_mfma_f32_16x16x32_bf16 v[68:71], v[226:229], v[166:169], 0
	v_mfma_f32_16x16x32_bf16 v[64:67], v[234:237], v[166:169], 0
	v_mfma_f32_16x16x32_bf16 v[52:55], v[226:229], v[178:181], 0
	v_mfma_f32_16x16x32_bf16 v[48:51], v[234:237], v[178:181], 0
	v_mfma_f32_16x16x32_bf16 v[44:47], v[226:229], v[208:211], 0
	v_mfma_f32_16x16x32_bf16 v[40:43], v[234:237], v[208:211], 0
	v_mfma_f32_16x16x32_bf16 v[36:39], v[226:229], v[218:221], 0
	v_mfma_f32_16x16x32_bf16 v[32:35], v[234:237], v[218:221], 0
	v_mfma_f32_16x16x32_bf16 v[68:71], v[230:233], v[174:177], v[68:71]
	v_mfma_f32_16x16x32_bf16 v[64:67], v[238:241], v[174:177], v[64:67]
	v_mfma_f32_16x16x32_bf16 v[52:55], v[230:233], v[204:207], v[52:55]
	v_mfma_f32_16x16x32_bf16 v[48:51], v[238:241], v[204:207], v[48:51]
	v_mfma_f32_16x16x32_bf16 v[44:47], v[230:233], v[214:217], v[44:47]
	v_mfma_f32_16x16x32_bf16 v[40:43], v[238:241], v[214:217], v[40:43]
	v_mfma_f32_16x16x32_bf16 v[36:39], v[230:233], v[222:225], v[36:39]
	v_mfma_f32_16x16x32_bf16 v[32:35], v[238:241], v[222:225], v[32:35]
	s_setprio 0
	s_mov_b32 m0, s23
	s_barrier
	ds_read_b128 v[166:169], v185 offset:16384
	ds_read_b128 v[174:177], v185 offset:17408
	ds_read_b128 v[178:181], v185 offset:18432
	ds_read_b128 v[204:207], v185 offset:19456
	ds_read_b128 v[208:211], v185 offset:20480
	ds_read_b128 v[214:217], v185 offset:21504
	ds_read_b128 v[218:221], v185 offset:22528
	ds_read_b128 v[222:225], v185 offset:23552
	global_load_lds_dwordx4 v172, s[30:31]
	s_mov_b32 m0, s56
	v_mov_b32_e32 v141, v173
	global_load_lds_dwordx4 v140, s[30:31]
	s_barrier
	s_waitcnt lgkmcnt(0)
	v_lshl_add_u64 v[196:197], s[30:31], 0, v[172:173]
	v_lshl_add_u64 v[242:243], s[30:31], 0, v[140:141]
	s_setprio 1
	s_waitcnt lgkmcnt(0)
	v_mfma_f32_16x16x32_bf16 v[92:95], v[142:145], v[166:169], 0
	v_mfma_f32_16x16x32_bf16 v[88:91], v[150:153], v[166:169], 0
	v_mfma_f32_16x16x32_bf16 v[84:87], v[142:145], v[178:181], 0
	v_mfma_f32_16x16x32_bf16 v[80:83], v[150:153], v[178:181], 0
	v_mfma_f32_16x16x32_bf16 v[76:79], v[142:145], v[208:211], 0
	v_mfma_f32_16x16x32_bf16 v[72:75], v[150:153], v[208:211], 0
	v_mfma_f32_16x16x32_bf16 v[60:63], v[142:145], v[218:221], 0
	v_mfma_f32_16x16x32_bf16 v[56:59], v[150:153], v[218:221], 0
	v_mfma_f32_16x16x32_bf16 v[92:95], v[146:149], v[174:177], v[92:95]
	v_mfma_f32_16x16x32_bf16 v[88:91], v[162:165], v[174:177], v[88:91]
	v_mfma_f32_16x16x32_bf16 v[84:87], v[146:149], v[204:207], v[84:87]
	v_mfma_f32_16x16x32_bf16 v[80:83], v[162:165], v[204:207], v[80:83]
	v_mfma_f32_16x16x32_bf16 v[76:79], v[146:149], v[214:217], v[76:79]
	v_mfma_f32_16x16x32_bf16 v[72:75], v[162:165], v[214:217], v[72:75]
	v_mfma_f32_16x16x32_bf16 v[60:63], v[146:149], v[222:225], v[60:63]
	v_mfma_f32_16x16x32_bf16 v[56:59], v[162:165], v[222:225], v[56:59]
	s_setprio 0
	s_barrier
	s_add_u32 s94, s28, 0x40000
	s_addc_u32 s95, s29, 0
	s_mov_b32 m0, s65
	v_lshl_add_u64 v[140:141], s[94:95], 0, v[158:159]
	global_load_lds_dwordx4 v[140:141], off
	v_lshl_add_u64 v[140:141], s[94:95], 0, v[160:161]
	s_mov_b32 m0, s70
	s_nop 0
	global_load_lds_dwordx4 v[140:141], off
	s_waitcnt vmcnt(6)
	s_barrier
	s_setprio 1
	v_mfma_f32_16x16x32_bf16 v[28:31], v[226:229], v[166:169], 0
	v_mfma_f32_16x16x32_bf16 v[24:27], v[234:237], v[166:169], 0
	v_mfma_f32_16x16x32_bf16 v[20:23], v[226:229], v[178:181], 0
	v_mfma_f32_16x16x32_bf16 v[16:19], v[234:237], v[178:181], 0
	v_mfma_f32_16x16x32_bf16 v[12:15], v[226:229], v[208:211], 0
	v_mfma_f32_16x16x32_bf16 v[8:11], v[234:237], v[208:211], 0
	v_mfma_f32_16x16x32_bf16 v[4:7], v[226:229], v[218:221], 0
	v_mfma_f32_16x16x32_bf16 v[0:3], v[234:237], v[218:221], 0
	v_mfma_f32_16x16x32_bf16 v[28:31], v[230:233], v[174:177], v[28:31]
	v_mfma_f32_16x16x32_bf16 v[24:27], v[238:241], v[174:177], v[24:27]
	v_mfma_f32_16x16x32_bf16 v[20:23], v[230:233], v[204:207], v[20:23]
	v_mfma_f32_16x16x32_bf16 v[16:19], v[238:241], v[204:207], v[16:19]
	v_mfma_f32_16x16x32_bf16 v[12:15], v[230:233], v[214:217], v[12:15]
	v_mfma_f32_16x16x32_bf16 v[8:11], v[238:241], v[214:217], v[8:11]
	v_mfma_f32_16x16x32_bf16 v[4:7], v[230:233], v[222:225], v[4:7]
	v_mfma_f32_16x16x32_bf16 v[0:3], v[238:241], v[222:225], v[0:3]
	s_setprio 0
	s_barrier
	ds_read_b128 v[140:143], v186 offset:32768
	ds_read_b128 v[144:147], v186 offset:33792
	ds_read_b128 v[148:151], v186 offset:34816
	ds_read_b128 v[152:155], v186 offset:35840
	s_mov_b32 m0, s71
	v_lshl_add_u64 v[138:139], s[30:31], 0, v[138:139]
	ds_read_b128 v[162:165], v185 offset:32768
	ds_read_b128 v[166:169], v185 offset:33792
	ds_read_b128 v[174:177], v185 offset:34816
	ds_read_b128 v[178:181], v185 offset:35840
	ds_read_b128 v[204:207], v185 offset:36864
	ds_read_b128 v[208:211], v185 offset:37888
	ds_read_b128 v[214:217], v185 offset:38912
	ds_read_b128 v[218:221], v185 offset:39936
	global_load_lds_dwordx4 v[138:139], off
	v_lshl_add_u64 v[136:137], s[30:31], 0, v[136:137]
	s_mov_b32 m0, s80
	s_nop 0
	global_load_lds_dwordx4 v[136:137], off
	s_waitcnt lgkmcnt(8)
	s_barrier
	s_waitcnt lgkmcnt(0)
	s_setprio 1
	s_waitcnt lgkmcnt(0)
	v_mfma_f32_16x16x32_bf16 v[124:127], v[140:143], v[162:165], v[124:127]
	v_mfma_f32_16x16x32_bf16 v[120:123], v[148:151], v[162:165], v[120:123]
	v_mfma_f32_16x16x32_bf16 v[116:119], v[140:143], v[174:177], v[116:119]
	v_mfma_f32_16x16x32_bf16 v[112:115], v[148:151], v[174:177], v[112:115]
	v_mfma_f32_16x16x32_bf16 v[108:111], v[140:143], v[204:207], v[108:111]
	v_mfma_f32_16x16x32_bf16 v[104:107], v[148:151], v[204:207], v[104:107]
	v_mfma_f32_16x16x32_bf16 v[100:103], v[140:143], v[214:217], v[100:103]
	v_mfma_f32_16x16x32_bf16 v[96:99], v[148:151], v[214:217], v[96:99]
	v_mfma_f32_16x16x32_bf16 v[124:127], v[144:147], v[166:169], v[124:127]
	v_mfma_f32_16x16x32_bf16 v[120:123], v[152:155], v[166:169], v[120:123]
	v_mfma_f32_16x16x32_bf16 v[116:119], v[144:147], v[178:181], v[116:119]
	v_mfma_f32_16x16x32_bf16 v[112:115], v[152:155], v[178:181], v[112:115]
	v_mfma_f32_16x16x32_bf16 v[108:111], v[144:147], v[208:211], v[108:111]
	v_mfma_f32_16x16x32_bf16 v[104:107], v[152:155], v[208:211], v[104:107]
	v_mfma_f32_16x16x32_bf16 v[100:103], v[144:147], v[218:221], v[100:103]
	v_mfma_f32_16x16x32_bf16 v[96:99], v[152:155], v[218:221], v[96:99]
	s_setprio 0
	s_barrier
	s_mov_b32 m0, s81
	v_lshl_add_u64 v[170:171], v[170:171], 0, s[40:41]
	ds_read_b128 v[136:139], v186 offset:49152
	ds_read_b128 v[222:225], v186 offset:50176
	ds_read_b128 v[226:229], v186 offset:51200
	ds_read_b128 v[230:233], v186 offset:52224
	global_load_lds_dwordx4 v[170:171], off
	v_lshl_add_u64 v[170:171], v[182:183], 0, s[40:41]
	s_mov_b32 m0, s82
	s_nop 0
	global_load_lds_dwordx4 v[170:171], off
	s_barrier
	s_waitcnt lgkmcnt(0)
	s_setprio 1
	s_waitcnt lgkmcnt(0)
	v_mfma_f32_16x16x32_bf16 v[68:71], v[136:139], v[162:165], v[68:71]
	v_mfma_f32_16x16x32_bf16 v[64:67], v[226:229], v[162:165], v[64:67]
	v_mfma_f32_16x16x32_bf16 v[52:55], v[136:139], v[174:177], v[52:55]
	v_mfma_f32_16x16x32_bf16 v[48:51], v[226:229], v[174:177], v[48:51]
	v_mfma_f32_16x16x32_bf16 v[44:47], v[136:139], v[204:207], v[44:47]
	v_mfma_f32_16x16x32_bf16 v[40:43], v[226:229], v[204:207], v[40:43]
	v_mfma_f32_16x16x32_bf16 v[36:39], v[136:139], v[214:217], v[36:39]
	v_mfma_f32_16x16x32_bf16 v[32:35], v[226:229], v[214:217], v[32:35]
	v_mfma_f32_16x16x32_bf16 v[68:71], v[222:225], v[166:169], v[68:71]
	v_mfma_f32_16x16x32_bf16 v[64:67], v[230:233], v[166:169], v[64:67]
	v_mfma_f32_16x16x32_bf16 v[52:55], v[222:225], v[178:181], v[52:55]
	v_mfma_f32_16x16x32_bf16 v[48:51], v[230:233], v[178:181], v[48:51]
	v_mfma_f32_16x16x32_bf16 v[44:47], v[222:225], v[208:211], v[44:47]
	v_mfma_f32_16x16x32_bf16 v[40:43], v[230:233], v[208:211], v[40:43]
	v_mfma_f32_16x16x32_bf16 v[36:39], v[222:225], v[218:221], v[36:39]
	v_mfma_f32_16x16x32_bf16 v[32:35], v[230:233], v[218:221], v[32:35]
	s_setprio 0
	s_mov_b32 m0, s83
	v_lshl_add_u64 v[170:171], v[196:197], 0, s[40:41]
	s_barrier
	ds_read_b128 v[162:165], v185 offset:49152
	ds_read_b128 v[166:169], v185 offset:50176
	ds_read_b128 v[174:177], v185 offset:51200
	ds_read_b128 v[178:181], v185 offset:52224
	ds_read_b128 v[204:207], v185 offset:53248
	ds_read_b128 v[208:211], v185 offset:54272
	ds_read_b128 v[214:217], v185 offset:55296
	ds_read_b128 v[218:221], v185 offset:56320
	global_load_lds_dwordx4 v[170:171], off
	v_lshl_add_u64 v[170:171], v[242:243], 0, s[40:41]
	s_mov_b32 m0, s85
	s_nop 0
	global_load_lds_dwordx4 v[170:171], off
	s_barrier
	s_waitcnt lgkmcnt(0)
	s_setprio 1
	s_waitcnt lgkmcnt(0)
	v_mfma_f32_16x16x32_bf16 v[92:95], v[140:143], v[162:165], v[92:95]
	v_mfma_f32_16x16x32_bf16 v[88:91], v[148:151], v[162:165], v[88:91]
	v_mfma_f32_16x16x32_bf16 v[84:87], v[140:143], v[174:177], v[84:87]
	v_mfma_f32_16x16x32_bf16 v[80:83], v[148:151], v[174:177], v[80:83]
	v_mfma_f32_16x16x32_bf16 v[76:79], v[140:143], v[204:207], v[76:79]
	v_mfma_f32_16x16x32_bf16 v[72:75], v[148:151], v[204:207], v[72:75]
	v_mfma_f32_16x16x32_bf16 v[60:63], v[140:143], v[214:217], v[60:63]
	v_mfma_f32_16x16x32_bf16 v[56:59], v[148:151], v[214:217], v[56:59]
	v_mfma_f32_16x16x32_bf16 v[92:95], v[144:147], v[166:169], v[92:95]
	v_mfma_f32_16x16x32_bf16 v[88:91], v[152:155], v[166:169], v[88:91]
	v_mfma_f32_16x16x32_bf16 v[84:87], v[144:147], v[178:181], v[84:87]
	v_mfma_f32_16x16x32_bf16 v[80:83], v[152:155], v[178:181], v[80:83]
	v_mfma_f32_16x16x32_bf16 v[76:79], v[144:147], v[208:211], v[76:79]
	v_mfma_f32_16x16x32_bf16 v[72:75], v[152:155], v[208:211], v[72:75]
	v_mfma_f32_16x16x32_bf16 v[60:63], v[144:147], v[218:221], v[60:63]
	v_mfma_f32_16x16x32_bf16 v[56:59], v[152:155], v[218:221], v[56:59]
	s_setprio 0
	s_barrier
	s_add_u32 s28, s28, 0x40080
	s_addc_u32 s29, s29, 0
	s_mov_b32 m0, s87
	v_lshl_add_u64 v[140:141], s[28:29], 0, v[158:159]
	global_load_lds_dwordx4 v[140:141], off
	v_lshl_add_u64 v[140:141], s[28:29], 0, v[160:161]
	s_mov_b32 m0, s44
	s_nop 0
	global_load_lds_dwordx4 v[140:141], off
	s_waitcnt vmcnt(6)
	s_barrier
	s_setprio 1
	v_mfma_f32_16x16x32_bf16 v[28:31], v[136:139], v[162:165], v[28:31]
	v_mfma_f32_16x16x32_bf16 v[24:27], v[226:229], v[162:165], v[24:27]
	v_mfma_f32_16x16x32_bf16 v[20:23], v[136:139], v[174:177], v[20:23]
	v_mfma_f32_16x16x32_bf16 v[16:19], v[226:229], v[174:177], v[16:19]
	v_mfma_f32_16x16x32_bf16 v[12:15], v[136:139], v[204:207], v[12:15]
	v_mfma_f32_16x16x32_bf16 v[8:11], v[226:229], v[204:207], v[8:11]
	v_mfma_f32_16x16x32_bf16 v[4:7], v[136:139], v[214:217], v[4:7]
	v_mfma_f32_16x16x32_bf16 v[0:3], v[226:229], v[214:217], v[0:3]
	v_mfma_f32_16x16x32_bf16 v[28:31], v[222:225], v[166:169], v[28:31]
	v_mfma_f32_16x16x32_bf16 v[24:27], v[230:233], v[166:169], v[24:27]
	v_mfma_f32_16x16x32_bf16 v[20:23], v[222:225], v[178:181], v[20:23]
	v_mfma_f32_16x16x32_bf16 v[16:19], v[230:233], v[178:181], v[16:19]
	v_mfma_f32_16x16x32_bf16 v[12:15], v[222:225], v[208:211], v[12:15]
	v_mfma_f32_16x16x32_bf16 v[8:11], v[230:233], v[208:211], v[8:11]
	v_mfma_f32_16x16x32_bf16 v[4:7], v[222:225], v[218:221], v[4:7]
	v_mfma_f32_16x16x32_bf16 v[0:3], v[230:233], v[218:221], v[0:3]
	s_setprio 0
	s_add_i32 vcc_lo, vcc_lo, 2
	s_add_u32 s26, s26, 0x100
	s_addc_u32 s27, s27, 0
	s_add_u32 s9, s9, 0x100
	s_addc_u32 s15, s15, 0
	s_cmp_gt_u32 vcc_lo, 13
	s_barrier
	s_branch .LBB0_1320

.Lpeel_gu:
	s_mov_b64 s[24:25], 0
	v_mov_b32_e32 v186, v166
	v_mov_b32_e32 v184, v170
	v_mov_b64_e32 v[178:179], v[168:169]
	v_mov_b64_e32 v[176:177], v[174:175]
	ds_read_b128 v[0:3], v191
	ds_read_b128 v[8:11], v191 offset:2048
	ds_read_b128 v[4:7], v193
	ds_read_b128 v[12:15], v193 offset:2048
	s_add_u32 s26, s22, 0x80
	s_addc_u32 s27, s23, 0
	s_and_b64 s[24:25], s[24:25], exec
	s_cselect_b32 s27, s19, s27
	s_cselect_b32 s26, s18, s26
	s_cselect_b32 s25, s17, s3
	s_cselect_b32 s24, s16, s2
	v_lshl_add_u64 v[16:17], s[22:23], 0, v[168:169]
	s_add_i32 m0, s44, 0xc000
	ds_read_b128 v[226:229], v190
	ds_read_b128 v[234:237], v190 offset:2048
	ds_read_b128 v[230:233], v192
	ds_read_b128 v[238:241], v192 offset:2048
	ds_read_b128 v[242:245], v190 offset:4096
	ds_read_b128 v[204:207], v190 offset:6144
	ds_read_b128 v[246:249], v192 offset:4096
	ds_read_b128 v[208:211], v192 offset:6144
	global_load_lds_dwordx4 v[16:17], off
	v_lshl_add_u64 v[16:17], s[22:23], 0, v[174:175]
	s_add_i32 m0, s44, 0xe000
	s_nop 0
	global_load_lds_dwordx4 v[16:17], off
	s_waitcnt lgkmcnt(8)
	s_barrier
	s_waitcnt lgkmcnt(0)
	s_setprio 1
	s_waitcnt lgkmcnt(0)
	v_mfma_scale_f32_16x16x128_f8f6f4 v[156:159], v[0:7], v[226:233], 0, v189, v189 op_sel_hi:[0,0,0]
	v_mfma_scale_f32_16x16x128_f8f6f4 v[148:151], v[8:15], v[226:233], 0, v189, v189 op_sel_hi:[0,0,0]
	v_mfma_scale_f32_16x16x128_f8f6f4 v[140:143], v[0:7], v[234:241], 0, v189, v189 op_sel_hi:[0,0,0]
	v_mfma_scale_f32_16x16x128_f8f6f4 v[132:135], v[8:15], v[234:241], 0, v189, v189 op_sel_hi:[0,0,0]
	v_mfma_scale_f32_16x16x128_f8f6f4 v[124:127], v[0:7], v[242:249], 0, v189, v189 op_sel_hi:[0,0,0]
	v_mfma_scale_f32_16x16x128_f8f6f4 v[116:119], v[8:15], v[242:249], 0, v189, v189 op_sel_hi:[0,0,0]
	v_mfma_scale_f32_16x16x128_f8f6f4 v[108:111], v[0:7], v[204:211], 0, v189, v189 op_sel_hi:[0,0,0]
	v_mfma_scale_f32_16x16x128_f8f6f4 v[100:103], v[8:15], v[204:211], 0, v189, v189 op_sel_hi:[0,0,0]
	s_setprio 0
	s_barrier
	s_mov_b32 m0, s46
	v_lshl_add_u64 v[180:181], s[24:25], 0, v[160:161]
	ds_read_b128 v[16:19], v191 offset:16384
	ds_read_b128 v[24:27], v191 offset:18432
	ds_read_b128 v[20:23], v193 offset:16384
	ds_read_b128 v[28:31], v193 offset:18432
	global_load_lds_dwordx4 v[180:181], off
	v_lshl_add_u64 v[182:183], s[24:25], 0, v[162:163]
	s_mov_b32 m0, s47
	s_nop 0
	global_load_lds_dwordx4 v[182:183], off
	s_barrier
	s_waitcnt lgkmcnt(0)
	s_setprio 1
	s_waitcnt lgkmcnt(0)
	v_mfma_scale_f32_16x16x128_f8f6f4 v[152:155], v[16:23], v[226:233], 0, v189, v189 op_sel_hi:[0,0,0]
	v_mfma_scale_f32_16x16x128_f8f6f4 v[144:147], v[24:31], v[226:233], 0, v189, v189 op_sel_hi:[0,0,0]
	v_mfma_scale_f32_16x16x128_f8f6f4 v[136:139], v[16:23], v[234:241], 0, v189, v189 op_sel_hi:[0,0,0]
	v_mfma_scale_f32_16x16x128_f8f6f4 v[128:131], v[24:31], v[234:241], 0, v189, v189 op_sel_hi:[0,0,0]
	v_mfma_scale_f32_16x16x128_f8f6f4 v[120:123], v[16:23], v[242:249], 0, v189, v189 op_sel_hi:[0,0,0]
	v_mfma_scale_f32_16x16x128_f8f6f4 v[112:115], v[24:31], v[242:249], 0, v189, v189 op_sel_hi:[0,0,0]
	v_mfma_scale_f32_16x16x128_f8f6f4 v[104:107], v[16:23], v[204:211], 0, v189, v189 op_sel_hi:[0,0,0]
	v_mfma_scale_f32_16x16x128_f8f6f4 v[96:99], v[24:31], v[204:211], 0, v189, v189 op_sel_hi:[0,0,0]
	s_setprio 0
	s_mov_b32 m0, s44
	s_barrier
	ds_read_b128 v[204:207], v190 offset:16384
	ds_read_b128 v[226:229], v190 offset:18432
	ds_read_b128 v[208:211], v192 offset:16384
	ds_read_b128 v[230:233], v192 offset:18432
	ds_read_b128 v[234:237], v190 offset:20480
	ds_read_b128 v[242:245], v190 offset:22528
	ds_read_b128 v[238:241], v192 offset:20480
	ds_read_b128 v[246:249], v192 offset:22528
	global_load_lds_dwordx4 v186, s[26:27]
	s_mov_b32 m0, s50
	v_mov_b32_e32 v187, v173
	global_load_lds_dwordx4 v184, s[26:27]
	s_barrier
	s_waitcnt lgkmcnt(0)
	v_mov_b32_e32 v185, v173
	v_lshl_add_u64 v[186:187], s[26:27], 0, v[186:187]
	v_lshl_add_u64 v[184:185], s[26:27], 0, v[184:185]
	s_setprio 1
	s_waitcnt lgkmcnt(0)
	v_mfma_scale_f32_16x16x128_f8f6f4 v[92:95], v[0:7], v[204:211], 0, v189, v189 op_sel_hi:[0,0,0]
	v_mfma_scale_f32_16x16x128_f8f6f4 v[84:87], v[8:15], v[204:211], 0, v189, v189 op_sel_hi:[0,0,0]
	v_mfma_scale_f32_16x16x128_f8f6f4 v[76:79], v[0:7], v[226:233], 0, v189, v189 op_sel_hi:[0,0,0]
	v_mfma_scale_f32_16x16x128_f8f6f4 v[68:71], v[8:15], v[226:233], 0, v189, v189 op_sel_hi:[0,0,0]
	v_mfma_scale_f32_16x16x128_f8f6f4 v[60:63], v[0:7], v[234:241], 0, v189, v189 op_sel_hi:[0,0,0]
	v_mfma_scale_f32_16x16x128_f8f6f4 v[52:55], v[8:15], v[234:241], 0, v189, v189 op_sel_hi:[0,0,0]
	v_mfma_scale_f32_16x16x128_f8f6f4 v[44:47], v[0:7], v[242:249], 0, v189, v189 op_sel_hi:[0,0,0]
	v_mfma_scale_f32_16x16x128_f8f6f4 v[36:39], v[8:15], v[242:249], 0, v189, v189 op_sel_hi:[0,0,0]
	s_setprio 0
	s_barrier
	s_add_u32 s72, s24, 0x20000
	s_addc_u32 s73, s25, 0
	s_mov_b32 m0, s51
	v_lshl_add_u64 v[0:1], s[72:73], 0, v[160:161]
	global_load_lds_dwordx4 v[0:1], off
	v_lshl_add_u64 v[0:1], s[72:73], 0, v[162:163]
	s_mov_b32 m0, s56
	s_nop 0
	global_load_lds_dwordx4 v[0:1], off
	s_waitcnt vmcnt(6)
	s_barrier
	s_setprio 1
	v_mfma_scale_f32_16x16x128_f8f6f4 v[88:91], v[16:23], v[204:211], 0, v189, v189 op_sel_hi:[0,0,0]
	v_mfma_scale_f32_16x16x128_f8f6f4 v[80:83], v[24:31], v[204:211], 0, v189, v189 op_sel_hi:[0,0,0]
	v_mfma_scale_f32_16x16x128_f8f6f4 v[72:75], v[16:23], v[226:233], 0, v189, v189 op_sel_hi:[0,0,0]
	v_mfma_scale_f32_16x16x128_f8f6f4 v[64:67], v[24:31], v[226:233], 0, v189, v189 op_sel_hi:[0,0,0]
	v_mfma_scale_f32_16x16x128_f8f6f4 v[56:59], v[16:23], v[234:241], 0, v189, v189 op_sel_hi:[0,0,0]
	v_mfma_scale_f32_16x16x128_f8f6f4 v[48:51], v[24:31], v[234:241], 0, v189, v189 op_sel_hi:[0,0,0]
	v_mfma_scale_f32_16x16x128_f8f6f4 v[40:43], v[16:23], v[242:249], 0, v189, v189 op_sel_hi:[0,0,0]
	v_mfma_scale_f32_16x16x128_f8f6f4 v[32:35], v[24:31], v[242:249], 0, v189, v189 op_sel_hi:[0,0,0]
	s_setprio 0
	s_barrier
	ds_read_b128 v[0:3], v191 offset:32768
	ds_read_b128 v[8:11], v191 offset:34816
	ds_read_b128 v[4:7], v193 offset:32768
	ds_read_b128 v[12:15], v193 offset:34816
	s_mov_b32 m0, s65
	v_lshl_add_u64 v[178:179], s[26:27], 0, v[178:179]
	ds_read_b128 v[16:19], v190 offset:32768
	ds_read_b128 v[24:27], v190 offset:34816
	ds_read_b128 v[20:23], v192 offset:32768
	ds_read_b128 v[28:31], v192 offset:34816
	ds_read_b128 v[204:207], v190 offset:36864
	ds_read_b128 v[226:229], v190 offset:38912
	ds_read_b128 v[208:211], v192 offset:36864
	ds_read_b128 v[230:233], v192 offset:38912
	global_load_lds_dwordx4 v[178:179], off
	v_lshl_add_u64 v[176:177], s[26:27], 0, v[176:177]
	s_mov_b32 m0, s70
	s_nop 0
	global_load_lds_dwordx4 v[176:177], off
	s_waitcnt lgkmcnt(8)
	s_barrier
	s_waitcnt lgkmcnt(0)
	s_setprio 1
	s_waitcnt lgkmcnt(0)
	v_mfma_scale_f32_16x16x128_f8f6f4 v[156:159], v[0:7], v[16:23], v[156:159], v189, v189 op_sel_hi:[0,0,0]
	v_mfma_scale_f32_16x16x128_f8f6f4 v[148:151], v[8:15], v[16:23], v[148:151], v189, v189 op_sel_hi:[0,0,0]
	v_mfma_scale_f32_16x16x128_f8f6f4 v[140:143], v[0:7], v[24:31], v[140:143], v189, v189 op_sel_hi:[0,0,0]
	v_mfma_scale_f32_16x16x128_f8f6f4 v[132:135], v[8:15], v[24:31], v[132:135], v189, v189 op_sel_hi:[0,0,0]
	v_mfma_scale_f32_16x16x128_f8f6f4 v[124:127], v[0:7], v[204:211], v[124:127], v189, v189 op_sel_hi:[0,0,0]
	v_mfma_scale_f32_16x16x128_f8f6f4 v[116:119], v[8:15], v[204:211], v[116:119], v189, v189 op_sel_hi:[0,0,0]
	v_mfma_scale_f32_16x16x128_f8f6f4 v[108:111], v[0:7], v[226:233], v[108:111], v189, v189 op_sel_hi:[0,0,0]
	v_mfma_scale_f32_16x16x128_f8f6f4 v[100:103], v[8:15], v[226:233], v[100:103], v189, v189 op_sel_hi:[0,0,0]
	s_setprio 0
	s_barrier
	s_mov_b32 m0, s71
	v_lshl_add_u64 v[176:177], v[180:181], 0, s[40:41]
	ds_read_b128 v[234:237], v191 offset:49152
	ds_read_b128 v[242:245], v191 offset:51200
	ds_read_b128 v[238:241], v193 offset:49152
	ds_read_b128 v[246:249], v193 offset:51200
	global_load_lds_dwordx4 v[176:177], off
	v_lshl_add_u64 v[176:177], v[182:183], 0, s[40:41]
	s_mov_b32 m0, s80
	s_nop 0
	global_load_lds_dwordx4 v[176:177], off
	s_barrier
	s_waitcnt lgkmcnt(0)
	s_setprio 1
	s_waitcnt lgkmcnt(0)
	v_mfma_scale_f32_16x16x128_f8f6f4 v[152:155], v[234:241], v[16:23], v[152:155], v189, v189 op_sel_hi:[0,0,0]
	v_mfma_scale_f32_16x16x128_f8f6f4 v[144:147], v[242:249], v[16:23], v[144:147], v189, v189 op_sel_hi:[0,0,0]
	v_mfma_scale_f32_16x16x128_f8f6f4 v[136:139], v[234:241], v[24:31], v[136:139], v189, v189 op_sel_hi:[0,0,0]
	v_mfma_scale_f32_16x16x128_f8f6f4 v[128:131], v[242:249], v[24:31], v[128:131], v189, v189 op_sel_hi:[0,0,0]
	v_mfma_scale_f32_16x16x128_f8f6f4 v[120:123], v[234:241], v[204:211], v[120:123], v189, v189 op_sel_hi:[0,0,0]
	v_mfma_scale_f32_16x16x128_f8f6f4 v[112:115], v[242:249], v[204:211], v[112:115], v189, v189 op_sel_hi:[0,0,0]
	v_mfma_scale_f32_16x16x128_f8f6f4 v[104:107], v[234:241], v[226:233], v[104:107], v189, v189 op_sel_hi:[0,0,0]
	v_mfma_scale_f32_16x16x128_f8f6f4 v[96:99], v[242:249], v[226:233], v[96:99], v189, v189 op_sel_hi:[0,0,0]
	s_setprio 0
	s_mov_b32 m0, s81
	v_lshl_add_u64 v[186:187], v[186:187], 0, s[40:41]
	s_barrier
	ds_read_b128 v[16:19], v190 offset:49152
	ds_read_b128 v[24:27], v190 offset:51200
	ds_read_b128 v[20:23], v192 offset:49152
	ds_read_b128 v[28:31], v192 offset:51200
	ds_read_b128 v[176:179], v190 offset:53248
	ds_read_b128 v[204:207], v190 offset:55296
	ds_read_b128 v[180:183], v192 offset:53248
	ds_read_b128 v[208:211], v192 offset:55296
	global_load_lds_dwordx4 v[186:187], off
	v_lshl_add_u64 v[184:185], v[184:185], 0, s[40:41]
	s_mov_b32 m0, s82
	s_nop 0
	global_load_lds_dwordx4 v[184:185], off
	s_barrier
	s_waitcnt lgkmcnt(0)
	s_setprio 1
	s_waitcnt lgkmcnt(0)
	v_mfma_scale_f32_16x16x128_f8f6f4 v[92:95], v[0:7], v[16:23], v[92:95], v189, v189 op_sel_hi:[0,0,0]
	v_mfma_scale_f32_16x16x128_f8f6f4 v[84:87], v[8:15], v[16:23], v[84:87], v189, v189 op_sel_hi:[0,0,0]
	v_mfma_scale_f32_16x16x128_f8f6f4 v[76:79], v[0:7], v[24:31], v[76:79], v189, v189 op_sel_hi:[0,0,0]
	v_mfma_scale_f32_16x16x128_f8f6f4 v[68:71], v[8:15], v[24:31], v[68:71], v189, v189 op_sel_hi:[0,0,0]
	v_mfma_scale_f32_16x16x128_f8f6f4 v[60:63], v[0:7], v[176:183], v[60:63], v189, v189 op_sel_hi:[0,0,0]
	v_mfma_scale_f32_16x16x128_f8f6f4 v[52:55], v[8:15], v[176:183], v[52:55], v189, v189 op_sel_hi:[0,0,0]
	v_mfma_scale_f32_16x16x128_f8f6f4 v[44:47], v[0:7], v[204:211], v[44:47], v189, v189 op_sel_hi:[0,0,0]
	v_mfma_scale_f32_16x16x128_f8f6f4 v[36:39], v[8:15], v[204:211], v[36:39], v189, v189 op_sel_hi:[0,0,0]
	s_setprio 0
	s_barrier
	s_add_u32 s24, s24, 0x20080
	s_addc_u32 s25, s25, 0
	s_mov_b32 m0, s83
	v_lshl_add_u64 v[0:1], s[24:25], 0, v[160:161]
	global_load_lds_dwordx4 v[0:1], off
	v_lshl_add_u64 v[0:1], s[24:25], 0, v[162:163]
	s_mov_b32 m0, s85
	s_nop 0
	global_load_lds_dwordx4 v[0:1], off
	s_waitcnt vmcnt(6)
	s_barrier
	s_setprio 1
	v_mfma_scale_f32_16x16x128_f8f6f4 v[88:91], v[234:241], v[16:23], v[88:91], v189, v189 op_sel_hi:[0,0,0]
	v_mfma_scale_f32_16x16x128_f8f6f4 v[80:83], v[242:249], v[16:23], v[80:83], v189, v189 op_sel_hi:[0,0,0]
	v_mfma_scale_f32_16x16x128_f8f6f4 v[72:75], v[234:241], v[24:31], v[72:75], v189, v189 op_sel_hi:[0,0,0]
	v_mfma_scale_f32_16x16x128_f8f6f4 v[64:67], v[242:249], v[24:31], v[64:67], v189, v189 op_sel_hi:[0,0,0]
	v_mfma_scale_f32_16x16x128_f8f6f4 v[56:59], v[234:241], v[176:183], v[56:59], v189, v189 op_sel_hi:[0,0,0]
	v_mfma_scale_f32_16x16x128_f8f6f4 v[48:51], v[242:249], v[176:183], v[48:51], v189, v189 op_sel_hi:[0,0,0]
	v_mfma_scale_f32_16x16x128_f8f6f4 v[40:43], v[234:241], v[204:211], v[40:43], v189, v189 op_sel_hi:[0,0,0]
	v_mfma_scale_f32_16x16x128_f8f6f4 v[32:35], v[242:249], v[204:211], v[32:35], v189, v189 op_sel_hi:[0,0,0]
	s_setprio 0
	s_add_i32 s64, s64, 2
	s_add_u32 s22, s22, 0x100
	s_addc_u32 s23, s23, 0
	s_add_u32 s2, s2, 0x100
	s_addc_u32 s3, s3, 0
	s_cmp_gt_u32 s64, 5
	s_barrier
	s_branch .LBB0_1556

.Lpeel_dn:
	s_mov_b64 s[24:25], 0
	v_mov_b64_e32 v[176:177], v[170:171]
	v_mov_b64_e32 v[178:179], v[166:167]
	v_mov_b32_e32 v184, v174
	v_mov_b32_e32 v172, v168
	ds_read_b128 v[0:3], v190
	ds_read_b128 v[8:11], v190 offset:2048
	ds_read_b128 v[4:7], v192
	ds_read_b128 v[12:15], v192 offset:2048
	s_add_u32 s26, s22, 0x80
	s_addc_u32 s27, s23, 0
	s_and_b64 s[24:25], s[24:25], exec
	s_cselect_b32 s27, s19, s27
	s_cselect_b32 s26, s18, s26
	s_cselect_b32 s25, s17, s83
	s_cselect_b32 s24, s16, s7
	v_lshl_add_u64 v[16:17], s[22:23], 0, v[166:167]
	s_add_i32 m0, s13, 0xc000
	ds_read_b128 v[204:207], v189
	ds_read_b128 v[216:219], v189 offset:2048
	ds_read_b128 v[208:211], v191
	ds_read_b128 v[220:223], v191 offset:2048
	ds_read_b128 v[224:227], v189 offset:4096
	ds_read_b128 v[232:235], v189 offset:6144
	ds_read_b128 v[228:231], v191 offset:4096
	ds_read_b128 v[236:239], v191 offset:6144
	global_load_lds_dwordx4 v[16:17], off
	v_lshl_add_u64 v[16:17], s[22:23], 0, v[170:171]
	s_add_i32 m0, s13, 0xe000
	s_nop 0
	global_load_lds_dwordx4 v[16:17], off
	s_waitcnt lgkmcnt(8)
	s_barrier
	s_waitcnt lgkmcnt(0)
	s_setprio 1
	s_waitcnt lgkmcnt(0)
	v_mfma_scale_f32_16x16x128_f8f6f4 v[156:159], v[0:7], v[204:211], 0, v188, v188 op_sel_hi:[0,0,0]
	v_mfma_scale_f32_16x16x128_f8f6f4 v[152:155], v[8:15], v[204:211], 0, v188, v188 op_sel_hi:[0,0,0]
	v_mfma_scale_f32_16x16x128_f8f6f4 v[148:151], v[0:7], v[216:223], 0, v188, v188 op_sel_hi:[0,0,0]
	v_mfma_scale_f32_16x16x128_f8f6f4 v[144:147], v[8:15], v[216:223], 0, v188, v188 op_sel_hi:[0,0,0]
	v_mfma_scale_f32_16x16x128_f8f6f4 v[140:143], v[0:7], v[224:231], 0, v188, v188 op_sel_hi:[0,0,0]
	v_mfma_scale_f32_16x16x128_f8f6f4 v[136:139], v[8:15], v[224:231], 0, v188, v188 op_sel_hi:[0,0,0]
	v_mfma_scale_f32_16x16x128_f8f6f4 v[132:135], v[0:7], v[232:239], 0, v188, v188 op_sel_hi:[0,0,0]
	v_mfma_scale_f32_16x16x128_f8f6f4 v[128:131], v[8:15], v[232:239], 0, v188, v188 op_sel_hi:[0,0,0]
	s_setprio 0
	s_barrier
	s_mov_b32 m0, s15
	v_lshl_add_u64 v[180:181], s[24:25], 0, v[162:163]
	ds_read_b128 v[16:19], v190 offset:16384
	ds_read_b128 v[24:27], v190 offset:18432
	ds_read_b128 v[20:23], v192 offset:16384
	ds_read_b128 v[28:31], v192 offset:18432
	global_load_lds_dwordx4 v[180:181], off
	v_lshl_add_u64 v[182:183], s[24:25], 0, v[164:165]
	s_mov_b32 m0, s31
	s_nop 0
	global_load_lds_dwordx4 v[182:183], off
	s_barrier
	s_waitcnt lgkmcnt(0)
	s_setprio 1
	s_waitcnt lgkmcnt(0)
	v_mfma_scale_f32_16x16x128_f8f6f4 v[100:103], v[16:23], v[204:211], 0, v188, v188 op_sel_hi:[0,0,0]
	v_mfma_scale_f32_16x16x128_f8f6f4 v[96:99], v[24:31], v[204:211], 0, v188, v188 op_sel_hi:[0,0,0]
	v_mfma_scale_f32_16x16x128_f8f6f4 v[84:87], v[16:23], v[216:223], 0, v188, v188 op_sel_hi:[0,0,0]
	v_mfma_scale_f32_16x16x128_f8f6f4 v[80:83], v[24:31], v[216:223], 0, v188, v188 op_sel_hi:[0,0,0]
	v_mfma_scale_f32_16x16x128_f8f6f4 v[76:79], v[16:23], v[224:231], 0, v188, v188 op_sel_hi:[0,0,0]
	v_mfma_scale_f32_16x16x128_f8f6f4 v[72:75], v[24:31], v[224:231], 0, v188, v188 op_sel_hi:[0,0,0]
	v_mfma_scale_f32_16x16x128_f8f6f4 v[68:71], v[16:23], v[232:239], 0, v188, v188 op_sel_hi:[0,0,0]
	v_mfma_scale_f32_16x16x128_f8f6f4 v[64:67], v[24:31], v[232:239], 0, v188, v188 op_sel_hi:[0,0,0]
	s_setprio 0
	s_mov_b32 m0, s13
	s_barrier
	ds_read_b128 v[204:207], v189 offset:16384
	ds_read_b128 v[216:219], v189 offset:18432
	ds_read_b128 v[208:211], v191 offset:16384
	ds_read_b128 v[220:223], v191 offset:18432
	ds_read_b128 v[224:227], v189 offset:20480
	ds_read_b128 v[232:235], v189 offset:22528
	ds_read_b128 v[228:231], v191 offset:20480
	ds_read_b128 v[236:239], v191 offset:22528
	global_load_lds_dwordx4 v172, s[26:27]
	s_mov_b32 m0, s44
	v_mov_b32_e32 v185, v173
	global_load_lds_dwordx4 v184, s[26:27]
	s_barrier
	s_waitcnt lgkmcnt(0)
	v_lshl_add_u64 v[186:187], s[26:27], 0, v[172:173]
	v_lshl_add_u64 v[184:185], s[26:27], 0, v[184:185]
	s_setprio 1
	s_waitcnt lgkmcnt(0)
	v_mfma_scale_f32_16x16x128_f8f6f4 v[124:127], v[0:7], v[204:211], 0, v188, v188 op_sel_hi:[0,0,0]
	v_mfma_scale_f32_16x16x128_f8f6f4 v[120:123], v[8:15], v[204:211], 0, v188, v188 op_sel_hi:[0,0,0]
	v_mfma_scale_f32_16x16x128_f8f6f4 v[116:119], v[0:7], v[216:223], 0, v188, v188 op_sel_hi:[0,0,0]
	v_mfma_scale_f32_16x16x128_f8f6f4 v[112:115], v[8:15], v[216:223], 0, v188, v188 op_sel_hi:[0,0,0]
	v_mfma_scale_f32_16x16x128_f8f6f4 v[108:111], v[0:7], v[224:231], 0, v188, v188 op_sel_hi:[0,0,0]
	v_mfma_scale_f32_16x16x128_f8f6f4 v[104:107], v[8:15], v[224:231], 0, v188, v188 op_sel_hi:[0,0,0]
	v_mfma_scale_f32_16x16x128_f8f6f4 v[92:95], v[0:7], v[232:239], 0, v188, v188 op_sel_hi:[0,0,0]
	v_mfma_scale_f32_16x16x128_f8f6f4 v[88:91], v[8:15], v[232:239], 0, v188, v188 op_sel_hi:[0,0,0]
	s_setprio 0
	s_barrier
	s_add_u32 s90, s24, 0x20000
	s_addc_u32 s91, s25, 0
	s_mov_b32 m0, s46
	v_lshl_add_u64 v[0:1], s[90:91], 0, v[162:163]
	global_load_lds_dwordx4 v[0:1], off
	v_lshl_add_u64 v[0:1], s[90:91], 0, v[164:165]
	s_mov_b32 m0, s47
	s_nop 0
	global_load_lds_dwordx4 v[0:1], off
	s_waitcnt vmcnt(6)
	s_barrier
	s_setprio 1
	v_mfma_scale_f32_16x16x128_f8f6f4 v[60:63], v[16:23], v[204:211], 0, v188, v188 op_sel_hi:[0,0,0]
	v_mfma_scale_f32_16x16x128_f8f6f4 v[56:59], v[24:31], v[204:211], 0, v188, v188 op_sel_hi:[0,0,0]
	v_mfma_scale_f32_16x16x128_f8f6f4 v[52:55], v[16:23], v[216:223], 0, v188, v188 op_sel_hi:[0,0,0]
	v_mfma_scale_f32_16x16x128_f8f6f4 v[48:51], v[24:31], v[216:223], 0, v188, v188 op_sel_hi:[0,0,0]
	v_mfma_scale_f32_16x16x128_f8f6f4 v[44:47], v[16:23], v[224:231], 0, v188, v188 op_sel_hi:[0,0,0]
	v_mfma_scale_f32_16x16x128_f8f6f4 v[40:43], v[24:31], v[224:231], 0, v188, v188 op_sel_hi:[0,0,0]
	v_mfma_scale_f32_16x16x128_f8f6f4 v[36:39], v[16:23], v[232:239], 0, v188, v188 op_sel_hi:[0,0,0]
	v_mfma_scale_f32_16x16x128_f8f6f4 v[32:35], v[24:31], v[232:239], 0, v188, v188 op_sel_hi:[0,0,0]
	s_setprio 0
	s_barrier
	ds_read_b128 v[0:3], v190 offset:32768
	ds_read_b128 v[8:11], v190 offset:34816
	ds_read_b128 v[4:7], v192 offset:32768
	ds_read_b128 v[12:15], v192 offset:34816
	s_mov_b32 m0, s50
	v_lshl_add_u64 v[178:179], s[26:27], 0, v[178:179]
	ds_read_b128 v[16:19], v189 offset:32768
	ds_read_b128 v[24:27], v189 offset:34816
	ds_read_b128 v[20:23], v191 offset:32768
	ds_read_b128 v[28:31], v191 offset:34816
	ds_read_b128 v[204:207], v189 offset:36864
	ds_read_b128 v[216:219], v189 offset:38912
	ds_read_b128 v[208:211], v191 offset:36864
	ds_read_b128 v[220:223], v191 offset:38912
	global_load_lds_dwordx4 v[178:179], off
	v_lshl_add_u64 v[176:177], s[26:27], 0, v[176:177]
	s_mov_b32 m0, s51
	s_nop 0
	global_load_lds_dwordx4 v[176:177], off
	s_waitcnt lgkmcnt(8)
	s_barrier
	s_waitcnt lgkmcnt(0)
	s_setprio 1
	s_waitcnt lgkmcnt(0)
	v_mfma_scale_f32_16x16x128_f8f6f4 v[156:159], v[0:7], v[16:23], v[156:159], v188, v188 op_sel_hi:[0,0,0]
	v_mfma_scale_f32_16x16x128_f8f6f4 v[152:155], v[8:15], v[16:23], v[152:155], v188, v188 op_sel_hi:[0,0,0]
	v_mfma_scale_f32_16x16x128_f8f6f4 v[148:151], v[0:7], v[24:31], v[148:151], v188, v188 op_sel_hi:[0,0,0]
	v_mfma_scale_f32_16x16x128_f8f6f4 v[144:147], v[8:15], v[24:31], v[144:147], v188, v188 op_sel_hi:[0,0,0]
	v_mfma_scale_f32_16x16x128_f8f6f4 v[140:143], v[0:7], v[204:211], v[140:143], v188, v188 op_sel_hi:[0,0,0]
	v_mfma_scale_f32_16x16x128_f8f6f4 v[136:139], v[8:15], v[204:211], v[136:139], v188, v188 op_sel_hi:[0,0,0]
	v_mfma_scale_f32_16x16x128_f8f6f4 v[132:135], v[0:7], v[216:223], v[132:135], v188, v188 op_sel_hi:[0,0,0]
	v_mfma_scale_f32_16x16x128_f8f6f4 v[128:131], v[8:15], v[216:223], v[128:131], v188, v188 op_sel_hi:[0,0,0]
	s_setprio 0
	s_barrier
	s_mov_b32 m0, s56
	v_lshl_add_u64 v[176:177], v[180:181], 0, s[40:41]
	ds_read_b128 v[224:227], v190 offset:49152
	ds_read_b128 v[232:235], v190 offset:51200
	ds_read_b128 v[228:231], v192 offset:49152
	ds_read_b128 v[236:239], v192 offset:51200
	global_load_lds_dwordx4 v[176:177], off
	v_lshl_add_u64 v[176:177], v[182:183], 0, s[40:41]
	s_mov_b32 m0, s57
	s_nop 0
	global_load_lds_dwordx4 v[176:177], off
	s_barrier
	s_waitcnt lgkmcnt(0)
	s_setprio 1
	s_waitcnt lgkmcnt(0)
	v_mfma_scale_f32_16x16x128_f8f6f4 v[100:103], v[224:231], v[16:23], v[100:103], v188, v188 op_sel_hi:[0,0,0]
	v_mfma_scale_f32_16x16x128_f8f6f4 v[96:99], v[232:239], v[16:23], v[96:99], v188, v188 op_sel_hi:[0,0,0]
	v_mfma_scale_f32_16x16x128_f8f6f4 v[84:87], v[224:231], v[24:31], v[84:87], v188, v188 op_sel_hi:[0,0,0]
	v_mfma_scale_f32_16x16x128_f8f6f4 v[80:83], v[232:239], v[24:31], v[80:83], v188, v188 op_sel_hi:[0,0,0]
	v_mfma_scale_f32_16x16x128_f8f6f4 v[76:79], v[224:231], v[204:211], v[76:79], v188, v188 op_sel_hi:[0,0,0]
	v_mfma_scale_f32_16x16x128_f8f6f4 v[72:75], v[232:239], v[204:211], v[72:75], v188, v188 op_sel_hi:[0,0,0]
	v_mfma_scale_f32_16x16x128_f8f6f4 v[68:71], v[224:231], v[216:223], v[68:71], v188, v188 op_sel_hi:[0,0,0]
	v_mfma_scale_f32_16x16x128_f8f6f4 v[64:67], v[232:239], v[216:223], v[64:67], v188, v188 op_sel_hi:[0,0,0]
	s_setprio 0
	s_mov_b32 m0, s64
	v_lshl_add_u64 v[186:187], v[186:187], 0, s[40:41]
	s_barrier
	ds_read_b128 v[16:19], v189 offset:49152
	ds_read_b128 v[24:27], v189 offset:51200
	ds_read_b128 v[20:23], v191 offset:49152
	ds_read_b128 v[28:31], v191 offset:51200
	ds_read_b128 v[176:179], v189 offset:53248
	ds_read_b128 v[204:207], v189 offset:55296
	ds_read_b128 v[180:183], v191 offset:53248
	ds_read_b128 v[208:211], v191 offset:55296
	global_load_lds_dwordx4 v[186:187], off
	v_lshl_add_u64 v[184:185], v[184:185], 0, s[40:41]
	s_mov_b32 m0, s65
	s_nop 0
	global_load_lds_dwordx4 v[184:185], off
	s_barrier
	s_waitcnt lgkmcnt(0)
	s_setprio 1
	s_waitcnt lgkmcnt(0)
	v_mfma_scale_f32_16x16x128_f8f6f4 v[124:127], v[0:7], v[16:23], v[124:127], v188, v188 op_sel_hi:[0,0,0]
	v_mfma_scale_f32_16x16x128_f8f6f4 v[120:123], v[8:15], v[16:23], v[120:123], v188, v188 op_sel_hi:[0,0,0]
	v_mfma_scale_f32_16x16x128_f8f6f4 v[116:119], v[0:7], v[24:31], v[116:119], v188, v188 op_sel_hi:[0,0,0]
	v_mfma_scale_f32_16x16x128_f8f6f4 v[112:115], v[8:15], v[24:31], v[112:115], v188, v188 op_sel_hi:[0,0,0]
	v_mfma_scale_f32_16x16x128_f8f6f4 v[108:111], v[0:7], v[176:183], v[108:111], v188, v188 op_sel_hi:[0,0,0]
	v_mfma_scale_f32_16x16x128_f8f6f4 v[104:107], v[8:15], v[176:183], v[104:107], v188, v188 op_sel_hi:[0,0,0]
	v_mfma_scale_f32_16x16x128_f8f6f4 v[92:95], v[0:7], v[204:211], v[92:95], v188, v188 op_sel_hi:[0,0,0]
	v_mfma_scale_f32_16x16x128_f8f6f4 v[88:91], v[8:15], v[204:211], v[88:91], v188, v188 op_sel_hi:[0,0,0]
	s_setprio 0
	s_barrier
	s_add_u32 s24, s24, 0x20080
	s_addc_u32 s25, s25, 0
	s_mov_b32 m0, s70
	v_lshl_add_u64 v[0:1], s[24:25], 0, v[162:163]
	global_load_lds_dwordx4 v[0:1], off
	v_lshl_add_u64 v[0:1], s[24:25], 0, v[164:165]
	s_mov_b32 m0, s71
	s_nop 0
	global_load_lds_dwordx4 v[0:1], off
	s_waitcnt vmcnt(6)
	s_barrier
	s_setprio 1
	v_mfma_scale_f32_16x16x128_f8f6f4 v[60:63], v[224:231], v[16:23], v[60:63], v188, v188 op_sel_hi:[0,0,0]
	v_mfma_scale_f32_16x16x128_f8f6f4 v[56:59], v[232:239], v[16:23], v[56:59], v188, v188 op_sel_hi:[0,0,0]
	v_mfma_scale_f32_16x16x128_f8f6f4 v[52:55], v[224:231], v[24:31], v[52:55], v188, v188 op_sel_hi:[0,0,0]
	v_mfma_scale_f32_16x16x128_f8f6f4 v[48:51], v[232:239], v[24:31], v[48:51], v188, v188 op_sel_hi:[0,0,0]
	v_mfma_scale_f32_16x16x128_f8f6f4 v[44:47], v[224:231], v[176:183], v[44:47], v188, v188 op_sel_hi:[0,0,0]
	v_mfma_scale_f32_16x16x128_f8f6f4 v[40:43], v[232:239], v[176:183], v[40:43], v188, v188 op_sel_hi:[0,0,0]
	v_mfma_scale_f32_16x16x128_f8f6f4 v[36:39], v[224:231], v[204:211], v[36:39], v188, v188 op_sel_hi:[0,0,0]
	v_mfma_scale_f32_16x16x128_f8f6f4 v[32:35], v[232:239], v[204:211], v[32:35], v188, v188 op_sel_hi:[0,0,0]
	s_setprio 0
	s_add_i32 s85, s85, 2
	s_add_u32 s22, s22, 0x100
	s_addc_u32 s23, s23, 0
	s_add_u32 s7, s7, 0x100
	s_addc_u32 s83, s83, 0
	s_cmp_gt_u32 s85, 5
	s_barrier
	s_branch .LBB0_1667
